# lever: DPP / permlane for intra-wave movement instead of LDS round trips - norm1 row sum-of-squares all-reduce: six ds_bpermute+lgkmcnt(0) steps replaced by four DPP row steps and the permlane16/32 sw
# speedup vs baseline: 1.0039x; 1.0039x over previous
; __device__ __forceinline__ unsigned cvtpk(float lo, float hi) { f32x2 v = {lo, hi}; bf16x2_t b = __builtin_convertvector(v, bf16x2_t); return __builtin_bit_cast(unsigned, b); }
; __device__ __forceinline__ float wave_sum(float v) {
; #pragma unroll
;     for (int o = 1; o < 64; o <<= 1) v += __shfl_xor(v, o);
;     return v;
; __device__ __forceinline__ void norm1_phase(Frame& F, KArgs a, int L) {
;     ...
;             for (int j = 0; j < 4; ++j) *(f32x4*)(xr[k] + 256 * j + 4 * lane) = v[k][j];
;             if (L == 4) continue;
;             float sq = 0.f;
; #pragma unroll
;             for (int j = 0; j < 4; ++j) sq += (v[k][j][0] * v[k][j][0] + v[k][j][1] * v[k][j][1]) + (v[k][j][2] * v[k][j][2] + v[k][j][3] * v[k][j][3]);
;             const float rstd = rsqrtf(wave_sum(sq) * (1.f / DM) + EPS);
;             const float* sh = MOD + ((size_t)(L * 9 + ss[k]) * 6 + 0) * 1024; const float* scl = sh + 1024;
;             bf16_t* hr = H + (size_t)rw[k] * DM;
; #pragma unroll
;             for (int j = 0; j < 4; ++j) { const int c = 256 * j + 4 * lane; const f32x4 g = *(const f32x4*)(gnm + c), sf = *(const f32x4*)(sh + c), sc = *(const f32x4*)(scl + c);
;                 f32x4 h = (v[k][j] * rstd) * g * (sc + 1.f) + sf; u32x2 w; w.x = cvtpk(h[0], h[1]); w.y = cvtpk(h[2], h[3]); *(u32x2*)(hr + c) = w; }
.LBB0_170:
	s_add_i32 s4, s7, s70
	s_mul_hi_i32 s5, s4, 0x6000
	s_mulk_i32 s4, 0x6000
	s_add_u32 s4, s53, s4
	s_addc_u32 s5, s59, s5
	global_store_dwordx4 v194, v[14:17], s[36:37]
	global_store_dwordx4 v194, v[10:13], s[36:37] offset:1024
	global_store_dwordx4 v194, v[6:9], s[36:37] offset:2048
	global_store_dwordx4 v194, v[2:5], s[36:37] offset:3072
	s_add_u32 s30, s4, 0x1000
	global_load_dwordx4 v[18:21], v[42:43], off
	s_addc_u32 s31, s5, 0
	global_load_dwordx4 v[22:25], v194, s[30:31]
	global_load_dwordx4 v[26:29], v194, s[4:5]
	v_pk_mul_f32 v[30:31], v[16:17], v[16:17]
	v_pk_mul_f32 v[32:33], v[14:15], v[14:15]
	s_ashr_i32 s11, s10, 31
	v_pk_mov_b32 v[34:35], v[32:33], v[30:31] op_sel:[1,0]
	v_mov_b32_e32 v33, v31
	v_pk_add_f32 v[30:31], v[34:35], v[32:33]
	v_pk_mul_f32 v[32:33], v[12:13], v[12:13]
	v_pk_mul_f32 v[34:35], v[10:11], v[10:11]
	v_pk_add_f32 v[30:31], v[30:31], v[30:31] op_sel:[0,1] op_sel_hi:[1,0]
	v_pk_mov_b32 v[36:37], v[34:35], v[32:33] op_sel:[1,0]
	v_mov_b32_e32 v35, v33
	v_pk_add_f32 v[32:33], v[36:37], v[34:35]
	v_mul_f32_e32 v34, v2, v2
	v_mul_f32_e32 v35, v3, v3
	v_pk_add_f32 v[32:33], v[32:33], v[32:33] op_sel:[0,1] op_sel_hi:[1,0]
	v_mov_b32_e32 v31, v34
	v_mov_b32_e32 v33, v35
	v_pk_add_f32 v[30:31], v[30:31], v[32:33]
	v_mul_f32_e32 v32, v7, v7
	v_mul_f32_e32 v34, v9, v9
	v_mul_f32_e32 v36, v4, v4
	v_mul_f32_e32 v37, v5, v5
	v_pk_fma_f32 v[32:33], v[6:7], v[6:7], v[32:33] op_sel_hi:[1,1,0]
	v_pk_fma_f32 v[34:35], v[8:9], v[8:9], v[34:35] op_sel_hi:[1,1,0]
	v_mov_b32_e32 v33, v36
	v_mov_b32_e32 v35, v37
	v_pk_add_f32 v[32:33], v[32:33], v[34:35]
	s_lshl_b64 s[10:11], s[10:11], 11
	v_pk_add_f32 v[30:31], v[30:31], v[32:33]
	s_nop 0
	v_add_f32_e32 v30, v30, v31
	s_nop 1
	v_add_f32_dpp v30, v30, v30 quad_perm:[1,0,3,2] row_mask:0xf bank_mask:0xf
	s_nop 1
	v_add_f32_dpp v30, v30, v30 quad_perm:[2,3,0,1] row_mask:0xf bank_mask:0xf
	s_nop 1
	v_add_f32_dpp v30, v30, v30 row_half_mirror row_mask:0xf bank_mask:0xf
	s_nop 1
	v_add_f32_dpp v30, v30, v30 row_mirror row_mask:0xf bank_mask:0xf
	v_mov_b32_e32 v31, v30
	s_nop 1
	v_permlane16_swap_b32_e32 v30, v31
	v_add_f32_e32 v31, v30, v31
	v_mov_b32_e32 v30, v31
	s_nop 1
	v_permlane32_swap_b32_e32 v31, v30
	v_add_f32_e32 v30, v31, v30
	v_fmamk_f32 v30, v30, 0x3a800000, v196
	v_mul_f32_e32 v31, 0x4b800000, v30
	v_cmp_gt_f32_e32 vcc, s95, v30
	s_nop 1
	v_cndmask_b32_e32 v30, v30, v31, vcc
	v_rsq_f32_e32 v32, v30
	v_lshl_add_u64 v[30:31], v[44:45], 0, s[10:11]
	v_mul_f32_e32 v33, 0x45800000, v32
	v_cndmask_b32_e32 v32, v32, v33, vcc
	v_pk_mul_f32 v[16:17], v[16:17], v[32:33] op_sel_hi:[1,0]
	v_pk_mul_f32 v[14:15], v[14:15], v[32:33] op_sel_hi:[1,0]
	s_waitcnt vmcnt(2)
	v_pk_mul_f32 v[16:17], v[20:21], v[16:17]
	v_pk_mul_f32 v[14:15], v[18:19], v[14:15]
	s_waitcnt vmcnt(1)
	v_pk_add_f32 v[18:19], v[24:25], 1.0 op_sel_hi:[1,0]
	v_pk_add_f32 v[20:21], v[22:23], 1.0 op_sel_hi:[1,0]
	s_waitcnt vmcnt(0)
	v_pk_fma_f32 v[16:17], v[18:19], v[16:17], v[28:29]
	v_pk_fma_f32 v[14:15], v[20:21], v[14:15], v[26:27]
	v_pk_mul_f32 v[12:13], v[12:13], v[32:33] op_sel_hi:[1,0]
	v_cvt_pk_bf16_f32 v14, v14, v15
	v_cvt_pk_bf16_f32 v15, v16, v17
	global_store_dwordx2 v[30:31], v[14:15], off
	global_load_dwordx4 v[14:17], v[42:43], off offset:1024
	s_nop 0
	global_load_dwordx4 v[18:21], v95, s[30:31]
	global_load_dwordx4 v[22:25], v194, s[4:5] offset:1024
	v_pk_mul_f32 v[10:11], v[10:11], v[32:33] op_sel_hi:[1,0]
	v_pk_mul_f32 v[8:9], v[8:9], v[32:33] op_sel_hi:[1,0]
	v_pk_mul_f32 v[6:7], v[6:7], v[32:33] op_sel_hi:[1,0]
	v_pk_mul_f32 v[4:5], v[4:5], v[32:33] op_sel_hi:[1,0]
	v_pk_mul_f32 v[2:3], v[2:3], v[32:33] op_sel_hi:[1,0]
	s_waitcnt vmcnt(2)
	v_pk_mul_f32 v[10:11], v[14:15], v[10:11]
	v_pk_mul_f32 v[12:13], v[16:17], v[12:13]
	s_waitcnt vmcnt(1)
	v_pk_add_f32 v[14:15], v[20:21], 1.0 op_sel_hi:[1,0]
	v_pk_add_f32 v[16:17], v[18:19], 1.0 op_sel_hi:[1,0]
	s_waitcnt vmcnt(0)
	v_pk_fma_f32 v[12:13], v[14:15], v[12:13], v[24:25]
	v_pk_fma_f32 v[10:11], v[16:17], v[10:11], v[22:23]
	s_nop 0
	v_cvt_pk_bf16_f32 v10, v10, v11
	v_cvt_pk_bf16_f32 v11, v12, v13
	global_store_dwordx2 v[30:31], v[10:11], off offset:512
	global_load_dwordx4 v[10:13], v[42:43], off offset:2048
	s_nop 0
	global_load_dwordx4 v[14:17], v96, s[30:31]
	global_load_dwordx4 v[18:21], v194, s[4:5] offset:2048
	s_waitcnt vmcnt(2)
	v_pk_mul_f32 v[6:7], v[10:11], v[6:7]
	v_pk_mul_f32 v[8:9], v[12:13], v[8:9]
	s_waitcnt vmcnt(1)
	v_pk_add_f32 v[10:11], v[16:17], 1.0 op_sel_hi:[1,0]
	v_pk_add_f32 v[12:13], v[14:15], 1.0 op_sel_hi:[1,0]
	s_waitcnt vmcnt(0)
	v_pk_fma_f32 v[8:9], v[10:11], v[8:9], v[20:21]
	v_pk_fma_f32 v[6:7], v[12:13], v[6:7], v[18:19]
	s_nop 0
	v_cvt_pk_bf16_f32 v6, v6, v7
	v_cvt_pk_bf16_f32 v7, v8, v9
	global_store_dwordx2 v[30:31], v[6:7], off offset:1024
	global_load_dwordx4 v[6:9], v[42:43], off offset:3072
	s_nop 0
	global_load_dwordx4 v[10:13], v97, s[30:31]
	global_load_dwordx4 v[14:17], v194, s[4:5] offset:3072
	s_waitcnt vmcnt(2)
	v_pk_mul_f32 v[2:3], v[2:3], v[6:7]
	v_pk_mul_f32 v[4:5], v[4:5], v[8:9]
	s_waitcnt vmcnt(1)
	v_pk_add_f32 v[6:7], v[12:13], 1.0 op_sel_hi:[1,0]
	v_pk_add_f32 v[8:9], v[10:11], 1.0 op_sel_hi:[1,0]
	s_waitcnt vmcnt(0)
	v_pk_fma_f32 v[4:5], v[4:5], v[6:7], v[16:17]
	v_pk_fma_f32 v[2:3], v[2:3], v[8:9], v[14:15]
	s_nop 0
	v_cvt_pk_bf16_f32 v2, v2, v3
	v_cvt_pk_bf16_f32 v3, v4, v5
	global_store_dwordx2 v[30:31], v[2:3], off offset:1536

; __device__ __forceinline__ void norm1_phase(Frame& F, KArgs a, int L) {
;     ...
;         for (int k = 0; k < RB; ++k) {
;             if (!ok[k]) continue;
;             if (L > 0) {
;                 f32x4 acc[4];
; #pragma unroll
;                 for (int j = 0; j < 4; ++j) acc[j] = (f32x4){0.f, 0.f, 0.f, 0.f};
;                 unsigned mask = (unsigned)__ballot(sl[k] >= 0) & 0xffffu;
;                 while (mask) {
;                     int pq[4]; float gq[4]; const int nq = __builtin_popcount(mask);
; #pragma unroll
;                     for (int q = 0; q < 4; ++q) {
;                         if (mask) { const int e = __builtin_ctz(mask); mask &= mask - 1u; pq[q] = __builtin_amdgcn_readlane(sl[k], e); gq[q] = __uint_as_float(__builtin_amdgcn_readlane(__float_as_uint(af[k]), e)); }
;                         else { pq[q] = pq[0]; gq[q] = 0.f; }
;                     }
;                     u32x2 y[4][4];
; #pragma unroll
;                     for (int q = 0; q < 4; ++q)
;                         if (q < nq) {
; #pragma unroll
;                             for (int j = 0; j < 4; ++j) y[q][j] = *(const u32x2*)(Y + (size_t)pq[q] * DM + 256 * j + 4 * lane); }
; #pragma unroll
;                     for (int q = 0; q < 4; ++q)
;                         if (q < nq) {
; #pragma unroll
;                             for (int j = 0; j < 4; ++j) { acc[j][0] += gq[q] * bf_lo(y[q][j].x); acc[j][1] += gq[q] * bf_hi(y[q][j].x); acc[j][2] += gq[q] * bf_lo(y[q][j].y); acc[j][3] += gq[q] * bf_hi(y[q][j].y); } }
;                 }
;                 const float* m5 = MOD + ((size_t)((L - 1) * 9 + ss[k]) * 6 + 5) * 1024;
; #pragma unroll
;                 for (int j = 0; j < 4; ++j) v[k][j] += *(const f32x4*)(m5 + 256 * j + 4 * lane) * acc[j];
;             }
; #pragma unroll
;             for (int j = 0; j < 4; ++j) *(f32x4*)(xr[k] + 256 * j + 4 * lane) = v[k][j];
;             if (L == 4) continue;
;             float sq = 0.f;
; #pragma unroll
;             for (int j = 0; j < 4; ++j) sq += (v[k][j][0] * v[k][j][0] + v[k][j][1] * v[k][j][1]) + (v[k][j][2] * v[k][j][2] + v[k][j][3] * v[k][j][3]);
;             const float rstd = rsqrtf(wave_sum(sq) * (1.f / DM) + EPS);
;             const float* sh = MOD + ((size_t)(L * 9 + ss[k]) * 6 + 0) * 1024; const float* scl = sh + 1024;
;             bf16_t* hr = H + (size_t)rw[k] * DM;
; #pragma unroll
.LBB0_219:
	s_add_i32 s7, s7, s70
	s_mul_hi_i32 s11, s7, 0x6000
	s_mulk_i32 s7, 0x6000
	s_add_u32 s30, s53, s7
	s_addc_u32 s31, s59, s11
	s_waitcnt vmcnt(7)
	global_store_dwordx4 v194, v[30:33], s[46:47]
	s_waitcnt vmcnt(7)
	global_store_dwordx4 v194, v[26:29], s[46:47] offset:1024
	s_waitcnt vmcnt(7)
	global_store_dwordx4 v194, v[22:25], s[46:47] offset:2048
	s_waitcnt vmcnt(7)
	global_store_dwordx4 v194, v[18:21], s[46:47] offset:3072
	s_add_u32 s46, s30, 0x1000
	global_load_dwordx4 v[34:37], v[42:43], off
	s_addc_u32 s47, s31, 0
	global_load_dwordx4 v[70:73], v194, s[46:47]
	global_load_dwordx4 v[74:77], v194, s[30:31]
	v_pk_mul_f32 v[78:79], v[32:33], v[32:33]
	v_pk_mul_f32 v[80:81], v[30:31], v[30:31]
	s_ashr_i32 s7, s6, 31
	v_pk_mov_b32 v[82:83], v[80:81], v[78:79] op_sel:[1,0]
	v_mov_b32_e32 v81, v79
	v_pk_add_f32 v[78:79], v[82:83], v[80:81]
	v_pk_mul_f32 v[80:81], v[28:29], v[28:29]
	v_pk_mul_f32 v[82:83], v[26:27], v[26:27]
	v_pk_add_f32 v[78:79], v[78:79], v[78:79] op_sel:[0,1] op_sel_hi:[1,0]
	v_pk_mov_b32 v[84:85], v[82:83], v[80:81] op_sel:[1,0]
	v_mov_b32_e32 v83, v81
	v_pk_add_f32 v[80:81], v[84:85], v[82:83]
	v_mul_f32_e32 v82, v18, v18
	v_mul_f32_e32 v83, v19, v19
	v_pk_add_f32 v[80:81], v[80:81], v[80:81] op_sel:[0,1] op_sel_hi:[1,0]
	v_mov_b32_e32 v79, v83
	v_mov_b32_e32 v81, v82
	v_pk_add_f32 v[78:79], v[80:81], v[78:79]
	v_mul_f32_e32 v80, v23, v23
	v_mul_f32_e32 v82, v25, v25
	v_mul_f32_e32 v84, v20, v20
	v_mul_f32_e32 v85, v21, v21
	v_pk_fma_f32 v[80:81], v[22:23], v[22:23], v[80:81] op_sel_hi:[1,1,0]
	v_pk_fma_f32 v[82:83], v[24:25], v[24:25], v[82:83] op_sel_hi:[1,1,0]
	v_mov_b32_e32 v81, v84
	v_mov_b32_e32 v83, v85
	v_pk_add_f32 v[80:81], v[80:81], v[82:83]
	s_lshl_b64 s[48:49], s[6:7], 11
	v_pk_add_f32 v[78:79], v[78:79], v[80:81]
	s_nop 0
	v_add_f32_e32 v78, v78, v79
	s_nop 1
	v_add_f32_dpp v78, v78, v78 quad_perm:[1,0,3,2] row_mask:0xf bank_mask:0xf
	s_nop 1
	v_add_f32_dpp v78, v78, v78 quad_perm:[2,3,0,1] row_mask:0xf bank_mask:0xf
	s_nop 1
	v_add_f32_dpp v78, v78, v78 row_half_mirror row_mask:0xf bank_mask:0xf
	s_nop 1
	v_add_f32_dpp v78, v78, v78 row_mirror row_mask:0xf bank_mask:0xf
	v_mov_b32_e32 v79, v78
	s_nop 1
	v_permlane16_swap_b32_e32 v78, v79
	v_add_f32_e32 v79, v78, v79
	v_mov_b32_e32 v78, v79
	s_nop 1
	v_permlane32_swap_b32_e32 v79, v78
	v_add_f32_e32 v78, v79, v78
	v_fmamk_f32 v78, v78, 0x3a800000, v196
	v_mul_f32_e32 v79, 0x4b800000, v78
	v_cmp_gt_f32_e32 vcc, s95, v78
	s_nop 1
	v_cndmask_b32_e32 v78, v78, v79, vcc
	v_rsq_f32_e32 v80, v78
	v_lshl_add_u64 v[78:79], v[44:45], 0, s[48:49]
	v_mul_f32_e32 v81, 0x45800000, v80
	v_cndmask_b32_e32 v80, v80, v81, vcc
	v_pk_mul_f32 v[32:33], v[32:33], v[80:81] op_sel_hi:[1,0]
	v_pk_mul_f32 v[30:31], v[30:31], v[80:81] op_sel_hi:[1,0]
	s_waitcnt vmcnt(2)
	v_pk_mul_f32 v[32:33], v[36:37], v[32:33]
	v_pk_mul_f32 v[30:31], v[34:35], v[30:31]
	s_waitcnt vmcnt(1)
	v_pk_add_f32 v[34:35], v[72:73], 1.0 op_sel_hi:[1,0]
	v_pk_add_f32 v[36:37], v[70:71], 1.0 op_sel_hi:[1,0]
	s_waitcnt vmcnt(0)
	v_pk_fma_f32 v[32:33], v[34:35], v[32:33], v[76:77]
	v_pk_fma_f32 v[30:31], v[36:37], v[30:31], v[74:75]
	v_pk_mul_f32 v[28:29], v[28:29], v[80:81] op_sel_hi:[1,0]
	v_cvt_pk_bf16_f32 v30, v30, v31
	v_cvt_pk_bf16_f32 v31, v32, v33
	global_store_dwordx2 v[78:79], v[30:31], off
	global_load_dwordx4 v[30:33], v[42:43], off offset:1024
	s_nop 0
	global_load_dwordx4 v[34:37], v95, s[46:47]
	global_load_dwordx4 v[70:73], v194, s[30:31] offset:1024
	v_pk_mul_f32 v[26:27], v[26:27], v[80:81] op_sel_hi:[1,0]
	v_pk_mul_f32 v[24:25], v[24:25], v[80:81] op_sel_hi:[1,0]
	v_pk_mul_f32 v[22:23], v[22:23], v[80:81] op_sel_hi:[1,0]
	v_pk_mul_f32 v[20:21], v[20:21], v[80:81] op_sel_hi:[1,0]
	v_pk_mul_f32 v[18:19], v[18:19], v[80:81] op_sel_hi:[1,0]
	s_andn2_b64 vcc, exec, s[40:41]
	s_waitcnt vmcnt(2)
	v_pk_mul_f32 v[26:27], v[30:31], v[26:27]
	v_pk_mul_f32 v[28:29], v[32:33], v[28:29]
	s_waitcnt vmcnt(1)
	v_pk_add_f32 v[30:31], v[36:37], 1.0 op_sel_hi:[1,0]
	v_pk_add_f32 v[32:33], v[34:35], 1.0 op_sel_hi:[1,0]
	s_waitcnt vmcnt(0)
	v_pk_fma_f32 v[28:29], v[30:31], v[28:29], v[72:73]
	v_pk_fma_f32 v[26:27], v[32:33], v[26:27], v[70:71]
	s_nop 0
	v_cvt_pk_bf16_f32 v26, v26, v27
	v_cvt_pk_bf16_f32 v27, v28, v29
	global_store_dwordx2 v[78:79], v[26:27], off offset:512
	global_load_dwordx4 v[26:29], v[42:43], off offset:2048
	s_nop 0
	global_load_dwordx4 v[30:33], v96, s[46:47]
	global_load_dwordx4 v[34:37], v194, s[30:31] offset:2048
	s_waitcnt vmcnt(2)
	v_pk_mul_f32 v[22:23], v[26:27], v[22:23]
	v_pk_mul_f32 v[24:25], v[28:29], v[24:25]
	s_waitcnt vmcnt(1)
	v_pk_add_f32 v[26:27], v[32:33], 1.0 op_sel_hi:[1,0]
	v_pk_add_f32 v[28:29], v[30:31], 1.0 op_sel_hi:[1,0]
	s_waitcnt vmcnt(0)
	v_pk_fma_f32 v[24:25], v[26:27], v[24:25], v[36:37]
	v_pk_fma_f32 v[22:23], v[28:29], v[22:23], v[34:35]
	s_nop 0
	v_cvt_pk_bf16_f32 v22, v22, v23
	v_cvt_pk_bf16_f32 v23, v24, v25
	global_store_dwordx2 v[78:79], v[22:23], off offset:1024
	global_load_dwordx4 v[22:25], v[42:43], off offset:3072
	s_nop 0
	global_load_dwordx4 v[26:29], v97, s[46:47]
	global_load_dwordx4 v[30:33], v194, s[30:31] offset:3072
	s_waitcnt vmcnt(2)
	v_pk_mul_f32 v[18:19], v[18:19], v[22:23]
	v_pk_mul_f32 v[20:21], v[20:21], v[24:25]
	s_waitcnt vmcnt(1)
	v_pk_add_f32 v[22:23], v[28:29], 1.0 op_sel_hi:[1,0]
	v_pk_add_f32 v[24:25], v[26:27], 1.0 op_sel_hi:[1,0]
	s_waitcnt vmcnt(0)
	v_pk_fma_f32 v[20:21], v[20:21], v[22:23], v[32:33]
	v_pk_fma_f32 v[18:19], v[18:19], v[24:25], v[30:31]
	s_nop 0
	v_cvt_pk_bf16_f32 v18, v18, v19
	v_cvt_pk_bf16_f32 v19, v20, v21
	global_store_dwordx2 v[78:79], v[18:19], off offset:1536
	s_cbranch_vccnz .LBB0_171
	s_and_b64 s[24:25], s[44:45], exec
	s_cselect_b32 s7, 8, s51
	s_and_b64 vcc, exec, s[4:5]
	s_cbranch_vccnz .LBB0_170
	v_cmp_lt_i32_e32 vcc, -1, v98
	s_and_b32 s11, vcc_lo, 0xffff
	s_cmp_eq_u32 s11, 0
	s_cbranch_scc1 .LBB0_168
	v_mov_b32_e32 v22, 0
	v_mov_b32_e32 v23, v22
	v_mov_b32_e32 v24, v22
	v_mov_b32_e32 v25, v22
	v_mov_b32_e32 v30, v22
	v_mov_b32_e32 v31, v22
	v_mov_b32_e32 v32, v22
	v_mov_b32_e32 v33, v22
	v_mov_b32_e32 v26, v22
	v_mov_b32_e32 v27, v22
	v_mov_b32_e32 v28, v22
	v_mov_b32_e32 v29, v22
	v_mov_b32_e32 v18, v22
	v_mov_b32_e32 v19, v22
	v_mov_b32_e32 v20, v22
	v_mov_b32_e32 v21, v22
